# E row loop: end-of-row wait leaves own write-through stores in flight (vmcnt 4/2 instead of 0)
# baseline (speedup 1.0000x reference)
; __device__ __forceinline__ float h_lo(unsigned u) { return (float)__builtin_bit_cast(f16v2, u)[0]; }
; __device__ __forceinline__ float h_hi(unsigned u) { return (float)__builtin_bit_cast(f16v2, u)[1]; }
; __device__ void phase_E_rows(const Params& p, int l, char* smem, int vb, int nvb, bool split, int nrows, int oz) {
;     ...
;     for (int row = rbeg; row < rend; ++row) {
;         const bool isctx = row >= LAT;
;         const int mr = isctx ? 8 : row / T;
;         if (mr != cur_mr) {
;             cur_mr = mr;
; #pragma unroll
;             for (int k = 0; k < 4; ++k) {
;                 const int col = (k >> 1) * 512 + lane * 8 + (k & 1) * 4;
;                 if (l > 0) {
;                     const float4 g = *(const float4*)(mod + ((l - 1) * 9 + mr) * 3072 + 2048 + col);
;                     const float4 pg = *(const float4*)(p.in[I_POSTG] + (l - 1) * DM + col);
;                     gp[k] = make_float4(g.x * pg.x, g.y * pg.y, g.z * pg.z, g.w * pg.w);
;                 }
;                 if (l < 4) {
;                     const float4 pre = *(const float4*)(p.in[I_PREG] + l * DM + col);
;                     const float4 sc = *(const float4*)(mod + (l * 9 + mr) * 3072 + 1024 + col);
;                     sh[k] = *(const float4*)(mod + (l * 9 + mr) * 3072 + col);
;                     pa[k] = make_float4(pre.x * (1.f + sc.x), pre.y * (1.f + sc.y), pre.z * (1.f + sc.z), pre.w * (1.f + sc.w));
;                 }
;             }
;         }
;         float* xcur = isctx ? XC + (size_t)(row - LAT) * DM : p.out + (size_t)row * DM;
;         float4 xv[4];
;         u32x4 yq[2];
; #pragma unroll
;         for (int k = 0; k < 4; ++k) {
;             const u32x4 w = nxb0[k >> 1];
;             const int h2 = 2 * (k & 1);
;             xv[k] = (l <= 1) ? nx0[k] : make_float4(h_lo(w[h2]), h_hi(w[h2]), h_lo(w[h2 + 1]), h_hi(w[h2 + 1]));
;         }
; #pragma unroll
;         for (int k = 0; k < 4; ++k) nx0[k] = nx1[k];
; #pragma unroll
;         for (int k2 = 0; k2 < 2; ++k2) { yq[k2] = ny0[k2]; nxb0[k2] = nxb1[k2]; ny0[k2] = ny1[k2]; }
;         if (row + 2 < rend) E2_LOAD(nx1, nxb1, ny1, row + 2)
.LBB0_964:
	s_add_u32 s56, s56, 1
	s_addc_u32 s57, s57, 0
	s_add_u32 s64, s64, 0x800
	s_addc_u32 s65, s65, 0
	s_cmp_lt_i32 s56, s27
	s_cbranch_scc0 .LBB0_841
	v_mov_b64_e32 v[44:45], v[84:85]
	v_mov_b64_e32 v[48:49], v[88:89]
	v_mov_b64_e32 v[20:21], v[92:93]
	v_mov_b64_e32 v[24:25], v[96:97]
	v_mov_b64_e32 v[46:47], v[86:87]
	v_mov_b64_e32 v[50:51], v[90:91]
	v_mov_b64_e32 v[22:23], v[94:95]
	v_mov_b64_e32 v[26:27], v[98:99]
	s_cmp_lg_u64 s[44:45], 0
	s_cbranch_scc1 .Le_row_l0
	s_waitcnt vmcnt(4)
	s_branch .Le_row_w
.Le_row_l0:
	s_waitcnt vmcnt(2)
.Le_row_w:
	v_mov_b64_e32 v[86:87], v[82:83]
	v_mov_b64_e32 v[90:91], v[74:75]
	v_mov_b64_e32 v[94:95], v[78:79]
	v_mov_b64_e32 v[98:99], v[70:71]
	v_mov_b64_e32 v[84:85], v[80:81]
	v_mov_b64_e32 v[88:89], v[72:73]
	v_mov_b64_e32 v[92:93], v[76:77]
	v_mov_b64_e32 v[96:97], v[68:69]
	s_mov_b32 s28, s66
	v_mov_b64_e32 v[38:39], v[160:161]
	v_mov_b64_e32 v[36:37], v[158:159]
	v_mov_b64_e32 v[42:43], v[164:165]
	v_mov_b64_e32 v[40:41], v[162:163]
	v_mov_b64_e32 v[30:31], v[152:153]
	v_mov_b64_e32 v[28:29], v[150:151]
	v_mov_b64_e32 v[34:35], v[156:157]
	v_mov_b64_e32 v[32:33], v[154:155]
	s_branch .LBB0_914
